# P0 three-way rotation by vcu mod 3: sections-then-MoE, MoE half / sections / MoE half, MoE-then-sections
# speedup vs baseline: 1.0008x; 1.0008x over previous
.LBB0_15:
	v_writelane_b32 v253, s10, 26
	s_load_dwordx16 s[4:19], s[0:1], 0x0
	s_waitcnt lgkmcnt(0)
	v_writelane_b32 v253, s4, 27
	s_nop 1
	v_writelane_b32 v253, s5, 28
	v_writelane_b32 v253, s6, 29
	v_writelane_b32 v253, s7, 30
	v_writelane_b32 v253, s8, 31
	v_writelane_b32 v253, s9, 32
	v_writelane_b32 v253, s10, 33
	v_writelane_b32 v253, s11, 34
	v_writelane_b32 v253, s12, 35
	v_writelane_b32 v253, s13, 36
	v_writelane_b32 v253, s14, 37
	v_writelane_b32 v253, s15, 38
	v_writelane_b32 v253, s16, 39
	v_writelane_b32 v253, s17, 40
	v_writelane_b32 v253, s18, 41
	v_writelane_b32 v253, s19, 42
	s_load_dwordx16 s[4:19], s[0:1], 0x40
	s_waitcnt lgkmcnt(0)
	v_writelane_b32 v253, s4, 43
	s_nop 1
	v_writelane_b32 v253, s5, 44
	v_writelane_b32 v253, s6, 45
	v_writelane_b32 v253, s7, 46
	v_writelane_b32 v253, s8, 47
	v_writelane_b32 v253, s9, 48
	v_writelane_b32 v253, s10, 49
	v_writelane_b32 v253, s11, 50
	v_writelane_b32 v253, s12, 51
	v_writelane_b32 v253, s13, 52
	v_writelane_b32 v253, s14, 53
	v_writelane_b32 v253, s15, 54
	v_writelane_b32 v253, s16, 55
	v_writelane_b32 v253, s17, 56
	v_writelane_b32 v253, s18, 57
	v_writelane_b32 v253, s19, 58
	s_load_dwordx2 s[6:7], s[0:1], 0x110
	s_waitcnt lgkmcnt(0)
	s_cmp_gt_i32 s6, 0
	s_cselect_b64 s[2:3], -1, 0
	s_cmp_lt_i32 s7, 1
	s_cselect_b64 s[4:5], -1, 0
	s_or_b64 s[2:3], s[2:3], s[4:5]
	s_and_b64 vcc, exec, s[2:3]
	s_cbranch_vccnz .LBB0_267
	s_mov_b32 s101, 0
	s_mov_b32 s99, 0x12000
.Lp0_body:
	s_cmp_lg_u32 s101, 0
	s_cbranch_scc1 .Lp0_sections
	v_readlane_b32 s39, v253, 3
	s_nop 3
	s_mul_i32 s2, s39, 0xaaab
	s_lshr_b32 s2, s2, 17
	s_mul_i32 s2, s2, 3
	s_sub_u32 s100, s39, s2
	s_cmp_eq_u32 s100, 0
	s_cbranch_scc1 .Lp0_sections
	s_mov_b32 s101, 1
	s_mov_b32 s99, 0x12000
	s_cmp_eq_u32 s100, 1
	s_cselect_b32 s99, 0x9000, s99
	v_mbcnt_lo_u32_b32 v99, -1, 0
	v_mbcnt_hi_u32_b32 v99, -1, v99
	v_readlane_b32 s1, v253, 20
	v_readlane_b32 s78, v253, 2
	s_nop 3
	s_lshl_b32 s0, s39, 3
	s_add_i32 s16, s0, s1
	s_lshl_b32 s8, s1, 14
	s_lshl_b32 s17, s78, 3
	v_lshlrev_b32_e32 v164, 3, v99
	v_ashrrev_i32_e32 v45, 3, v99
	v_and_b32_e32 v2, 7, v99
	v_mov_b32_e32 v33, 0
	v_ashrrev_i32_e32 v38, 3, v99
	v_lshlrev_b32_e32 v32, 2, v2
	v_and_b32_e32 v44, 24, v164
	v_lshlrev_b32_e32 v131, 11, v2
	v_lshlrev_b32_e32 v34, 4, v2
	v_mov_b32_e32 v35, v33
	s_branch .LBB0_205

.LBB0_205:
	s_cmp_eq_u32 s101, 2
	s_cbranch_scc0 .Lp0_go
	s_cmp_eq_u32 s100, 2
	s_cbranch_scc1 .Lp0_end
	s_mov_b32 s101, 3
	s_mov_b32 s99, 0x12000
	v_readlane_b32 s0, v253, 3
	v_readlane_b32 s1, v253, 20
	s_nop 3
	s_lshl_b32 s0, s0, 3
	s_add_i32 s0, s0, s1
	s_add_i32 s16, s0, 0x9000
.Lp0_go:
	s_cmp_lt_i32 s16, s99
	s_cselect_b64 s[0:1], -1, 0
	s_and_b64 vcc, exec, s[0:1]
	s_cbranch_vccz .LBB0_217
	s_add_i32 s2, s16, 0x4000
	s_cmp_lt_i32 s16, 0xc000
	s_cselect_b32 s2, s16, s2
	s_and_b64 s[0:1], exec, s[0:1]
	s_cselect_b32 s5, s2, 0
	s_ashr_i32 s0, s5, 31
	s_lshr_b32 s0, s0, 23
	s_add_i32 s6, s5, s0
	s_and_b32 s0, s6, 0xfffffe00
	s_sub_i32 s2, s5, s0
	s_and_b32 s3, s5, 0xff
	s_cmp_gt_i32 s5, 0xffff
	s_cselect_b64 s[0:1], -1, 0
	s_movk_i32 s4, 0x400
	s_and_b64 s[0:1], s[0:1], exec
	s_cselect_b32 s22, s4, 0x800
	s_cselect_b32 s0, s3, s2
	s_cselect_b32 s9, 10, 11
	s_lshr_b32 s4, s22, 5
	s_sext_i32_i16 s7, s4
	v_cvt_f32_i32_e32 v0, s7
	s_sext_i32_i16 s10, s0
	v_cvt_f32_i32_e32 v1, s10
	s_xor_b32 s7, s10, s7
	v_rcp_iflag_f32_e32 v2, v0
	s_ashr_i32 s7, s7, 30
	s_or_b32 s7, s7, 1
	s_mov_b32 s1, 0
	v_mul_f32_e32 v2, v1, v2
	v_trunc_f32_e32 v2, v2
	v_fma_f32 v1, -v2, v0, v1
	v_cvt_i32_f32_e32 v2, v2
	v_cmp_ge_f32_e64 s[2:3], |v1|, |v0|
	s_and_b64 s[2:3], s[2:3], exec
	s_cselect_b32 s2, s7, 0
	v_readfirstlane_b32 s3, v2
	s_add_i32 s14, s3, s2
	s_mul_i32 s2, s14, s4
	s_sub_i32 s0, s0, s2
	s_sext_i32_i16 s0, s0
	s_lshl_b32 s2, s0, 6
	s_lshl_b32 s4, s0, 5
	s_and_b32 s2, s2, 0x700
	s_cmp_gt_i32 s0, 31
	s_cselect_b32 s0, 0x80, 0
	s_or_b32 s0, s2, s0
	s_and_b32 s2, s4, 0x60
	s_or_b32 s0, s0, s2
	s_cmp_gt_i32 s5, 0xffff
	s_cselect_b64 s[2:3], -1, 0
	s_mov_b32 s7, 0x27600000
	s_and_b64 s[2:3], s[2:3], exec
	s_cselect_b32 s15, s7, 0x7600000
	s_cselect_b32 s23, s4, s0
	s_ashr_i32 s2, s6, 9
	s_add_i32 s0, s5, 0xffff0000
	s_ashr_i32 s3, s2, 31
	s_lshr_b32 s0, s0, 8
	s_lshl_b64 s[6:7], s[2:3], 21
	s_lshl_b64 s[10:11], s[0:1], 20
	s_cmp_gt_i32 s5, 0xffff
	s_cselect_b64 s[12:13], -1, 0
	s_and_b64 s[12:13], s[12:13], exec
	v_readlane_b32 s36, v253, 4
	s_cselect_b32 s6, s10, s6
	s_cselect_b32 s7, s11, s7
	s_lshl_b64 s[2:3], s[2:3], 23
	v_readlane_b32 s44, v253, 12
	v_readlane_b32 s45, v253, 13
	s_add_u32 s10, s44, s2
	v_readlane_b32 s48, v253, 16
	s_addc_u32 s11, s45, s3
	s_lshl_b64 s[2:3], s[0:1], 22
	v_readlane_b32 s49, v253, 17
	s_add_u32 s0, s48, s2
	s_addc_u32 s12, s49, s3
	s_cmp_gt_i32 s5, 0xffff
	s_cselect_b64 vcc, -1, 0
	s_and_b64 s[2:3], vcc, exec
	s_cselect_b32 s3, s12, s11
	s_cselect_b32 s2, s0, s10
	s_add_u32 s18, s94, 0x7600000
	s_addc_u32 s19, s95, 0
	s_add_u32 s20, s94, 0x27600000
	s_sext_i32_i16 s0, s14
	s_addc_u32 s21, s95, 0
	s_lshl_b32 s24, s0, 7
	s_add_u32 s0, s94, s15
	s_addc_u32 s5, s95, 0
	s_add_u32 s6, s0, s6
	s_addc_u32 s7, s5, s7
	v_add_u32_e32 v24, s24, v38
	s_ashr_i32 s5, s4, 31
	v_mov_b32_e32 v0, 0x43800000
	v_bfrev_b32_e32 v1, 34
	s_lshl_b64 s[10:11], s[4:5], 2
	v_ashrrev_i32_e32 v25, 31, v24
	v_cndmask_b32_e32 v41, v0, v1, vcc
	s_add_u32 s10, s2, s10
	v_lshlrev_b64 v[0:1], s9, v[24:25]
	v_add_u32_e32 v2, 8, v24
	v_add_u32_e32 v8, 16, v24
	v_add_u32_e32 v10, 24, v24
	v_add_u32_e32 v16, 32, v24
	v_add_u32_e32 v18, 40, v24
	v_add_u32_e32 v28, 48, v24
	v_add_u32_e32 v24, 56, v24
	s_addc_u32 s11, s3, s11
	v_ashrrev_i32_e32 v3, 31, v2
	v_ashrrev_i32_e32 v9, 31, v8
	v_ashrrev_i32_e32 v11, 31, v10
	v_ashrrev_i32_e32 v17, 31, v16
	v_ashrrev_i32_e32 v19, 31, v18
	v_ashrrev_i32_e32 v29, 31, v28
	v_ashrrev_i32_e32 v25, 31, v24
	v_lshl_add_u64 v[26:27], v[32:33], 2, s[10:11]
	v_lshlrev_b64 v[2:3], s9, v[2:3]
	v_lshlrev_b64 v[8:9], s9, v[8:9]
	v_lshlrev_b64 v[10:11], s9, v[10:11]
	v_lshlrev_b64 v[16:17], s9, v[16:17]
	v_lshlrev_b64 v[18:19], s9, v[18:19]
	v_lshlrev_b64 v[28:29], s9, v[28:29]
	v_lshlrev_b64 v[24:25], s9, v[24:25]
	v_lshl_add_u64 v[0:1], v[0:1], 2, v[26:27]
	v_lshl_add_u64 v[4:5], v[2:3], 2, v[26:27]
	v_lshl_add_u64 v[8:9], v[8:9], 2, v[26:27]
	v_lshl_add_u64 v[12:13], v[10:11], 2, v[26:27]
	v_lshl_add_u64 v[16:17], v[16:17], 2, v[26:27]
	v_lshl_add_u64 v[20:21], v[18:19], 2, v[26:27]
	v_lshl_add_u64 v[28:29], v[28:29], 2, v[26:27]
	v_lshl_add_u64 v[30:31], v[24:25], 2, v[26:27]
	global_load_dwordx4 v[0:3], v[0:1], off nt
	s_nop 0
	global_load_dwordx4 v[4:7], v[4:5], off nt
	s_nop 0
	global_load_dwordx4 v[8:11], v[8:9], off nt
	s_nop 0
	global_load_dwordx4 v[12:15], v[12:13], off nt
	s_nop 0
	global_load_dwordx4 v[16:19], v[16:17], off nt
	s_nop 0
	global_load_dwordx4 v[20:23], v[20:21], off nt
	s_nop 0
	global_load_dwordx4 v[24:27], v[28:29], off nt
	s_nop 0
	global_load_dwordx4 v[28:31], v[30:31], off nt
	v_lshrrev_b32_e32 v42, 1, v38
	v_or_b32_e32 v36, 3, v32
	v_or_b32_e32 v37, 2, v32
	v_or_b32_e32 v104, 1, v32
	v_and_b32_e32 v106, 7, v38
	v_and_b32_e32 v47, 24, v42
	v_bitop3_b32 v42, v47, v32, v106 bitop3:0x36
	v_bitop3_b32 v43, v47, v104, v106 bitop3:0x36
	v_bitop3_b32 v45, v47, v37, v106 bitop3:0x36
	v_bitop3_b32 v47, v47, v36, v106 bitop3:0x36
	v_lshlrev_b32_e32 v78, 2, v47
	v_add_u32_e32 v47, 8, v38
	v_lshl_add_u32 v50, v47, 7, s8
	v_lshrrev_b32_e32 v47, 1, v47
	v_and_b32_e32 v51, 24, v47
	v_bitop3_b32 v47, v51, v32, v106 bitop3:0x36
	v_bitop3_b32 v48, v51, v104, v106 bitop3:0x36
	v_bitop3_b32 v49, v51, v37, v106 bitop3:0x36
	v_bitop3_b32 v51, v51, v36, v106 bitop3:0x36
	v_lshl_add_u32 v47, v47, 2, v50
	v_lshl_add_u32 v48, v48, 2, v50
	v_lshl_add_u32 v49, v49, 2, v50
	v_lshl_add_u32 v50, v51, 2, v50
	v_add_u32_e32 v51, 16, v38
	v_lshl_add_u32 v54, v51, 7, s8
	v_lshrrev_b32_e32 v51, 1, v51
	v_and_b32_e32 v55, 24, v51
	v_bitop3_b32 v51, v55, v32, v106 bitop3:0x36
	v_bitop3_b32 v52, v55, v104, v106 bitop3:0x36
	v_bitop3_b32 v53, v55, v37, v106 bitop3:0x36
	v_bitop3_b32 v55, v55, v36, v106 bitop3:0x36
	v_lshl_add_u32 v51, v51, 2, v54
	v_lshl_add_u32 v52, v52, 2, v54
	v_lshl_add_u32 v53, v53, 2, v54
	v_lshl_add_u32 v54, v55, 2, v54
	v_add_u32_e32 v55, 24, v38
	v_lshl_add_u32 v58, v55, 7, s8
	v_lshrrev_b32_e32 v55, 1, v55
	v_and_b32_e32 v59, 24, v55
	v_bitop3_b32 v55, v59, v32, v106 bitop3:0x36
	v_bitop3_b32 v56, v59, v104, v106 bitop3:0x36
	v_bitop3_b32 v57, v59, v37, v106 bitop3:0x36
	v_bitop3_b32 v59, v59, v36, v106 bitop3:0x36
	v_lshl_add_u32 v55, v55, 2, v58
	v_lshl_add_u32 v56, v56, 2, v58
	v_lshl_add_u32 v57, v57, 2, v58
	v_lshl_add_u32 v58, v59, 2, v58
	v_add_u32_e32 v59, 32, v38
	v_lshl_add_u32 v62, v59, 7, s8
	v_lshrrev_b32_e32 v59, 1, v59
	v_and_b32_e32 v63, 24, v59
	v_bitop3_b32 v59, v63, v32, v106 bitop3:0x36
	v_bitop3_b32 v60, v63, v104, v106 bitop3:0x36
	v_bitop3_b32 v61, v63, v37, v106 bitop3:0x36
	v_bitop3_b32 v63, v63, v36, v106 bitop3:0x36
	v_lshl_add_u32 v59, v59, 2, v62
	v_lshl_add_u32 v60, v60, 2, v62
	v_lshl_add_u32 v61, v61, 2, v62
	v_lshl_add_u32 v62, v63, 2, v62
	v_add_u32_e32 v63, 40, v38
	v_lshl_add_u32 v66, v63, 7, s8
	v_lshrrev_b32_e32 v63, 1, v63
	v_and_b32_e32 v67, 24, v63
	v_bitop3_b32 v63, v67, v32, v106 bitop3:0x36
	v_bitop3_b32 v64, v67, v104, v106 bitop3:0x36
	v_bitop3_b32 v65, v67, v37, v106 bitop3:0x36
	v_bitop3_b32 v67, v67, v36, v106 bitop3:0x36
	v_lshl_add_u32 v63, v63, 2, v66
	v_lshl_add_u32 v64, v64, 2, v66
	v_lshl_add_u32 v65, v65, 2, v66
	v_lshl_add_u32 v66, v67, 2, v66
	v_add_u32_e32 v67, 48, v38
	v_lshl_add_u32 v70, v67, 7, s8
	v_lshrrev_b32_e32 v67, 1, v67
	v_and_b32_e32 v71, 24, v67
	v_bitop3_b32 v67, v71, v32, v106 bitop3:0x36
	v_bitop3_b32 v68, v71, v104, v106 bitop3:0x36
	v_bitop3_b32 v69, v71, v37, v106 bitop3:0x36
	v_bitop3_b32 v71, v71, v36, v106 bitop3:0x36
	v_lshl_add_u32 v67, v67, 2, v70
	v_lshl_add_u32 v68, v68, 2, v70
	v_lshl_add_u32 v69, v69, 2, v70
	v_lshl_add_u32 v70, v71, 2, v70
	v_add_u32_e32 v71, 56, v38
	v_lshl_add_u32 v74, v71, 7, s8
	v_lshrrev_b32_e32 v71, 1, v71
	v_and_b32_e32 v79, 24, v71
	v_add_u32_e32 v39, 64, v38
	v_bitop3_b32 v71, v79, v32, v106 bitop3:0x36
	v_bitop3_b32 v72, v79, v104, v106 bitop3:0x36
	v_bitop3_b32 v73, v79, v37, v106 bitop3:0x36
	v_bitop3_b32 v79, v79, v36, v106 bitop3:0x36
	v_lshl_add_u32 v46, v38, 7, s8
	v_lshlrev_b32_e32 v75, 2, v42
	v_lshlrev_b32_e32 v76, 2, v43
	v_lshlrev_b32_e32 v77, 2, v45
	v_lshl_add_u32 v71, v71, 2, v74
	v_lshl_add_u32 v72, v72, 2, v74
	v_lshl_add_u32 v73, v73, 2, v74
	v_lshl_add_u32 v74, v79, 2, v74
	v_lshl_add_u32 v79, v39, 7, s8
	v_add_u32_e32 v42, v46, v75
	v_add_u32_e32 v43, v46, v76
	v_add_u32_e32 v45, v46, v77
	v_add_u32_e32 v46, v46, v78
	v_add_u32_e32 v75, v79, v75
	v_add_u32_e32 v76, v79, v76
	v_add_u32_e32 v77, v79, v77
	v_add_u32_e32 v78, v79, v78
	v_add_u32_e32 v79, 0x48, v38
	v_lshl_add_u32 v82, v79, 7, s8
	v_lshrrev_b32_e32 v79, 1, v79
	v_and_b32_e32 v83, 24, v79
	v_bitop3_b32 v79, v83, v32, v106 bitop3:0x36
	v_bitop3_b32 v80, v83, v104, v106 bitop3:0x36
	v_bitop3_b32 v81, v83, v37, v106 bitop3:0x36
	v_bitop3_b32 v83, v83, v36, v106 bitop3:0x36
	v_lshl_add_u32 v79, v79, 2, v82
	v_lshl_add_u32 v80, v80, 2, v82
	v_lshl_add_u32 v81, v81, 2, v82
	v_lshl_add_u32 v82, v83, 2, v82
	v_add_u32_e32 v83, 0x50, v38
	v_lshl_add_u32 v86, v83, 7, s8
	v_lshrrev_b32_e32 v83, 1, v83
	v_and_b32_e32 v87, 24, v83
	v_bitop3_b32 v83, v87, v32, v106 bitop3:0x36
	v_bitop3_b32 v84, v87, v104, v106 bitop3:0x36
	v_bitop3_b32 v85, v87, v37, v106 bitop3:0x36
	v_bitop3_b32 v87, v87, v36, v106 bitop3:0x36
	v_lshl_add_u32 v83, v83, 2, v86
	v_lshl_add_u32 v84, v84, 2, v86
	v_lshl_add_u32 v85, v85, 2, v86
	v_lshl_add_u32 v86, v87, 2, v86
	v_add_u32_e32 v87, 0x58, v38
	v_lshl_add_u32 v90, v87, 7, s8
	v_lshrrev_b32_e32 v87, 1, v87
	v_and_b32_e32 v91, 24, v87
	v_bitop3_b32 v87, v91, v32, v106 bitop3:0x36
	v_bitop3_b32 v88, v91, v104, v106 bitop3:0x36
	v_bitop3_b32 v89, v91, v37, v106 bitop3:0x36
	v_bitop3_b32 v91, v91, v36, v106 bitop3:0x36
	v_lshl_add_u32 v87, v87, 2, v90
	v_lshl_add_u32 v88, v88, 2, v90
	v_lshl_add_u32 v89, v89, 2, v90
	v_lshl_add_u32 v90, v91, 2, v90
	v_add_u32_e32 v91, 0x60, v38
	v_lshl_add_u32 v94, v91, 7, s8
	v_lshrrev_b32_e32 v91, 1, v91
	v_and_b32_e32 v95, 24, v91
	v_bitop3_b32 v91, v95, v32, v106 bitop3:0x36
	v_bitop3_b32 v92, v95, v104, v106 bitop3:0x36
	v_bitop3_b32 v93, v95, v37, v106 bitop3:0x36
	v_bitop3_b32 v95, v95, v36, v106 bitop3:0x36
	v_lshl_add_u32 v91, v91, 2, v94
	v_lshl_add_u32 v92, v92, 2, v94
	v_lshl_add_u32 v93, v93, 2, v94
	v_lshl_add_u32 v94, v95, 2, v94
	v_add_u32_e32 v95, 0x68, v38
	v_lshl_add_u32 v98, v95, 7, s8
	v_lshrrev_b32_e32 v95, 1, v95
	v_and_b32_e32 v99, 24, v95
	v_bitop3_b32 v95, v99, v32, v106 bitop3:0x36
	v_bitop3_b32 v96, v99, v104, v106 bitop3:0x36
	v_bitop3_b32 v97, v99, v37, v106 bitop3:0x36
	v_bitop3_b32 v99, v99, v36, v106 bitop3:0x36
	v_lshl_add_u32 v95, v95, 2, v98
	v_lshl_add_u32 v96, v96, 2, v98
	v_lshl_add_u32 v97, v97, 2, v98
	v_lshl_add_u32 v98, v99, 2, v98
	v_add_u32_e32 v99, 0x70, v38
	v_lshl_add_u32 v102, v99, 7, s8
	v_lshrrev_b32_e32 v99, 1, v99
	v_and_b32_e32 v103, 24, v99
	v_bitop3_b32 v99, v103, v32, v106 bitop3:0x36
	v_bitop3_b32 v100, v103, v104, v106 bitop3:0x36
	v_bitop3_b32 v101, v103, v37, v106 bitop3:0x36
	v_bitop3_b32 v103, v103, v36, v106 bitop3:0x36
	v_lshl_add_u32 v99, v99, 2, v102
	v_lshl_add_u32 v100, v100, 2, v102
	v_lshl_add_u32 v101, v101, 2, v102
	v_lshl_add_u32 v102, v103, 2, v102
	v_add_u32_e32 v103, 0x78, v38
	v_lshl_add_u32 v107, v103, 7, s8
	v_lshrrev_b32_e32 v103, 1, v103
	v_and_b32_e32 v108, 24, v103
	v_bitop3_b32 v103, v108, v32, v106 bitop3:0x36
	v_bitop3_b32 v104, v108, v104, v106 bitop3:0x36
	v_bitop3_b32 v37, v108, v37, v106 bitop3:0x36
	v_bitop3_b32 v36, v108, v36, v106 bitop3:0x36
	v_add_u32_e32 v40, s8, v131
	v_lshl_add_u32 v103, v103, 2, v107
	v_lshl_add_u32 v104, v104, 2, v107
	v_lshl_add_u32 v105, v37, 2, v107
	v_lshl_add_u32 v106, v36, 2, v107
	v_or_b32_e32 v107, 1, v44
	v_or_b32_e32 v108, 2, v44
	v_or_b32_e32 v109, 3, v44
	v_or_b32_e32 v110, 4, v44
	v_or_b32_e32 v111, 5, v44
	v_or_b32_e32 v112, 6, v44
	v_or_b32_e32 v113, 7, v44
	s_mov_b32 s25, 0xc3e00000
	v_mov_b32_e32 v37, 0
	v_mov_b32_e32 v114, 0x43e00000
	v_readlane_b32 s37, v253, 5
	v_readlane_b32 s38, v253, 6
	v_readlane_b32 s39, v253, 7
	v_readlane_b32 s40, v253, 8
	v_readlane_b32 s41, v253, 9
	v_readlane_b32 s42, v253, 10
	v_readlane_b32 s43, v253, 11
	v_readlane_b32 s46, v253, 14
	v_readlane_b32 s47, v253, 15
	v_readlane_b32 s50, v253, 18
	v_readlane_b32 s51, v253, 19
.LBB0_207:
	s_ashr_i32 s5, s4, 31
	s_lshl_b64 s[4:5], s[4:5], 2
	s_add_u32 s2, s2, s4
	v_add_u32_e32 v115, s24, v39
	s_addc_u32 s3, s3, s5
	v_lshl_add_u64 v[144:145], v[32:33], 2, s[2:3]
	v_mad_u64_u32 v[116:117], s[2:3], v115, s22, 0
	v_ashrrev_i32_e32 v118, 31, v115
	v_mov_b32_e32 v36, v117
	v_mad_u64_u32 v[118:119], s[2:3], v118, s22, v[36:37]
	v_add_u32_e32 v36, 8, v115
	v_mov_b32_e32 v117, v118
	v_mad_u64_u32 v[118:119], s[2:3], v36, s22, 0
	v_ashrrev_i32_e32 v120, 31, v36
	v_mov_b32_e32 v36, v119
	v_mad_u64_u32 v[120:121], s[2:3], v120, s22, v[36:37]
	v_add_u32_e32 v36, 16, v115
	v_mad_u64_u32 v[124:125], s[2:3], v36, s22, 0
	v_ashrrev_i32_e32 v126, 31, v36
	v_mov_b32_e32 v36, v125
	v_mad_u64_u32 v[126:127], s[2:3], v126, s22, v[36:37]
	v_add_u32_e32 v36, 24, v115
	v_mov_b32_e32 v125, v126
	v_mad_u64_u32 v[126:127], s[2:3], v36, s22, 0
	v_ashrrev_i32_e32 v128, 31, v36
	v_mov_b32_e32 v36, v127
	v_mad_u64_u32 v[128:129], s[2:3], v128, s22, v[36:37]
	v_add_u32_e32 v36, 32, v115
	v_mad_u64_u32 v[132:133], s[2:3], v36, s22, 0
	v_ashrrev_i32_e32 v134, 31, v36
	v_mov_b32_e32 v36, v133
	v_mad_u64_u32 v[134:135], s[2:3], v134, s22, v[36:37]
	v_add_u32_e32 v36, 40, v115
	v_mov_b32_e32 v133, v134
	v_mad_u64_u32 v[134:135], s[2:3], v36, s22, 0
	v_ashrrev_i32_e32 v136, 31, v36
	v_mov_b32_e32 v36, v135
	v_mad_u64_u32 v[136:137], s[2:3], v136, s22, v[36:37]
	v_mov_b32_e32 v119, v120
	v_mov_b32_e32 v127, v128
	v_mov_b32_e32 v135, v136
	v_lshl_add_u64 v[116:117], v[116:117], 2, v[144:145]
	v_lshl_add_u64 v[120:121], v[118:119], 2, v[144:145]
	v_lshl_add_u64 v[124:125], v[124:125], 2, v[144:145]
	v_lshl_add_u64 v[128:129], v[126:127], 2, v[144:145]
	v_lshl_add_u64 v[132:133], v[132:133], 2, v[144:145]
	v_lshl_add_u64 v[136:137], v[134:135], 2, v[144:145]
	global_load_dwordx4 v[116:119], v[116:117], off nt
	s_nop 0
	global_load_dwordx4 v[120:123], v[120:121], off nt
	s_nop 0
	global_load_dwordx4 v[124:127], v[124:125], off nt
	s_nop 0
	global_load_dwordx4 v[128:131], v[128:129], off nt
	s_nop 0
	global_load_dwordx4 v[132:135], v[132:133], off nt
	s_nop 0
	global_load_dwordx4 v[136:139], v[136:137], off nt
	v_add_u32_e32 v36, 48, v115
	v_mad_u64_u32 v[140:141], s[2:3], v36, s22, 0
	v_ashrrev_i32_e32 v142, 31, v36
	v_mov_b32_e32 v36, v141
	v_mad_u64_u32 v[142:143], s[2:3], v142, s22, v[36:37]
	v_mov_b32_e32 v141, v142
	v_add_u32_e32 v36, 56, v115
	v_lshl_add_u64 v[140:141], v[140:141], 2, v[144:145]
	v_mad_u64_u32 v[146:147], s[2:3], v36, s22, 0
	global_load_dwordx4 v[140:143], v[140:141], off nt
	v_ashrrev_i32_e32 v115, 31, v36
	v_mov_b32_e32 v36, v147
	v_mad_u64_u32 v[148:149], s[2:3], v115, s22, v[36:37]
	v_mov_b32_e32 v147, v148
	v_lshl_add_u64 v[144:145], v[146:147], 2, v[144:145]
	global_load_dwordx4 v[144:147], v[144:145], off nt
	s_mov_b32 s0, s16
	s_add_i32 s16, s16, s17
	s_cmp_ge_i32 s16, s99
	s_cselect_b64 s[8:9], -1, 0
	s_cmp_lt_i32 s16, s99
	s_cselect_b64 s[14:15], -1, 0
	s_and_b64 s[2:3], s[14:15], exec
	s_cselect_b32 s0, s16, s0
	s_add_i32 s2, s0, 0x4000
	s_cmp_lt_i32 s0, 0xc000
	s_cselect_b32 s22, s0, s2
	s_cmp_gt_i32 s22, 0xffff
	s_cselect_b64 s[10:11], -1, 0
	s_mov_b64 s[4:5], -1
	s_and_b64 vcc, exec, s[10:11]
	s_waitcnt vmcnt(15)
	ds_write_b32 v42, v0
	ds_write_b32 v43, v1
	ds_write_b32 v45, v2
	ds_write_b32 v46, v3
	s_waitcnt vmcnt(14)
	ds_write_b32 v47, v4
	ds_write_b32 v48, v5
	ds_write_b32 v49, v6
	ds_write_b32 v50, v7
	s_waitcnt vmcnt(13)
	ds_write_b32 v51, v8
	ds_write_b32 v52, v9
	ds_write_b32 v53, v10
	ds_write_b32 v54, v11
	s_waitcnt vmcnt(12)
	ds_write_b32 v55, v12
	ds_write_b32 v56, v13
	ds_write_b32 v57, v14
	ds_write_b32 v58, v15
	s_waitcnt vmcnt(11)
	ds_write_b32 v59, v16
	ds_write_b32 v60, v17
	ds_write_b32 v61, v18
	ds_write_b32 v62, v19
	s_waitcnt vmcnt(10)
	ds_write_b32 v63, v20
	ds_write_b32 v64, v21
	ds_write_b32 v65, v22
	ds_write_b32 v66, v23
	s_waitcnt vmcnt(9)
	ds_write_b32 v67, v24
	ds_write_b32 v68, v25
	ds_write_b32 v69, v26
	ds_write_b32 v70, v27
	s_waitcnt vmcnt(8)
	ds_write_b32 v71, v28
	ds_write_b32 v72, v29
	ds_write_b32 v73, v30
	ds_write_b32 v74, v31
	s_waitcnt vmcnt(7)
	ds_write_b32 v75, v116
	ds_write_b32 v76, v117
	ds_write_b32 v77, v118
	ds_write_b32 v78, v119
	s_waitcnt vmcnt(6)
	ds_write_b32 v79, v120
	ds_write_b32 v80, v121
	ds_write_b32 v81, v122
	ds_write_b32 v82, v123
	s_waitcnt vmcnt(5)
	ds_write_b32 v83, v124
	ds_write_b32 v84, v125
	ds_write_b32 v85, v126
	ds_write_b32 v86, v127
	s_waitcnt vmcnt(4)
	ds_write_b32 v87, v128
	ds_write_b32 v88, v129
	ds_write_b32 v89, v130
	ds_write_b32 v90, v131
	s_waitcnt vmcnt(3)
	ds_write_b32 v91, v132
	ds_write_b32 v92, v133
	ds_write_b32 v93, v134
	ds_write_b32 v94, v135
	s_waitcnt vmcnt(2)
	ds_write_b32 v95, v136
	ds_write_b32 v96, v137
	ds_write_b32 v97, v138
	ds_write_b32 v98, v139
	s_waitcnt vmcnt(1)
	ds_write_b32 v99, v140
	ds_write_b32 v100, v141
	ds_write_b32 v101, v142
	ds_write_b32 v102, v143
	s_waitcnt vmcnt(0)
	ds_write_b32 v103, v144
	ds_write_b32 v104, v145
	ds_write_b32 v105, v146
	ds_write_b32 v106, v147
	s_cbranch_vccnz .LBB0_209
	s_ashr_i32 s0, s22, 31
	s_lshr_b32 s0, s0, 23
	s_add_i32 s0, s22, s0
	s_ashr_i32 s4, s0, 9
	s_and_b32 s0, s0, 0xfffffe00
	s_ashr_i32 s5, s4, 31
	v_readlane_b32 s36, v253, 4
	s_sub_i32 s26, s22, s0
	s_lshl_b64 s[2:3], s[4:5], 23
	v_readlane_b32 s44, v253, 12
	v_readlane_b32 s45, v253, 13
	s_add_u32 s2, s44, s2
	s_addc_u32 s3, s45, s3
	s_lshl_b64 s[4:5], s[4:5], 21
	s_add_u32 s12, s18, s4
	s_addc_u32 s13, s19, s5
	s_mov_b64 s[4:5], 0
	v_readlane_b32 s37, v253, 5
	v_readlane_b32 s38, v253, 6
	v_readlane_b32 s39, v253, 7
	v_readlane_b32 s40, v253, 8
	v_readlane_b32 s41, v253, 9
	v_readlane_b32 s42, v253, 10
	v_readlane_b32 s43, v253, 11
	v_readlane_b32 s46, v253, 14
	v_readlane_b32 s47, v253, 15
	v_readlane_b32 s48, v253, 16
	v_readlane_b32 s49, v253, 17
	v_readlane_b32 s50, v253, 18
	v_readlane_b32 s51, v253, 19
